# GQA fast loop: row sums as a 4-accumulator v_pk_add_f32 tree, no repeated vmcnt waits (K prefetch variant dropped)
# baseline (speedup 1.0000x reference)
.LBB0_881:
	ds_read_b128 v[96:99], v216 offset:49152
	ds_read_b128 v[100:103], v216 offset:57344
	ds_read_b128 v[178:181], v218 offset:49152
	ds_read_b128 v[182:185], v218 offset:57344
	s_waitcnt lgkmcnt(3)
	v_mfma_f32_32x32x16_bf16 v[112:127], v[96:99], v[138:141], 0
	s_waitcnt lgkmcnt(2)
	v_mfma_f32_32x32x16_bf16 v[96:111], v[100:103], v[138:141], 0
	s_waitcnt lgkmcnt(1)
	v_mfma_f32_32x32x16_bf16 v[112:127], v[178:181], v[154:157], v[112:127]
	s_waitcnt lgkmcnt(0)
	v_mfma_f32_32x32x16_bf16 v[96:111], v[182:185], v[154:157], v[96:111]
	ds_read_b128 v[178:181], v219 offset:49152
	ds_read_b128 v[182:185], v219 offset:57344
	s_waitcnt lgkmcnt(1)
	v_mfma_f32_32x32x16_bf16 v[112:127], v[178:181], v[158:161], v[112:127]
	s_waitcnt lgkmcnt(0)
	v_mfma_f32_32x32x16_bf16 v[96:111], v[182:185], v[158:161], v[96:111]
	ds_read_b128 v[178:181], v220 offset:49152
	ds_read_b128 v[182:185], v220 offset:57344
	s_waitcnt lgkmcnt(1)
	v_mfma_f32_32x32x16_bf16 v[112:127], v[178:181], v[150:153], v[112:127]
	s_waitcnt lgkmcnt(0)
	v_mfma_f32_32x32x16_bf16 v[96:111], v[182:185], v[150:153], v[96:111]
	ds_read_b128 v[178:181], v221 offset:49152
	ds_read_b128 v[182:185], v221 offset:57344
	s_waitcnt lgkmcnt(1)
	v_mfma_f32_32x32x16_bf16 v[112:127], v[178:181], v[146:149], v[112:127]
	s_waitcnt lgkmcnt(0)
	v_mfma_f32_32x32x16_bf16 v[96:111], v[182:185], v[146:149], v[96:111]
	ds_read_b128 v[178:181], v222 offset:49152
	ds_read_b128 v[182:185], v222 offset:57344
	s_waitcnt lgkmcnt(1)
	v_mfma_f32_32x32x16_bf16 v[112:127], v[178:181], v[142:145], v[112:127]
	s_waitcnt lgkmcnt(0)
	v_mfma_f32_32x32x16_bf16 v[96:111], v[182:185], v[142:145], v[96:111]
	ds_read_b128 v[178:181], v224 offset:49152
	ds_read_b128 v[182:185], v224 offset:57344
	s_waitcnt lgkmcnt(1)
	v_mfma_f32_32x32x16_bf16 v[112:127], v[178:181], v[134:137], v[112:127]
	s_waitcnt lgkmcnt(0)
	v_mfma_f32_32x32x16_bf16 v[96:111], v[182:185], v[134:137], v[96:111]
	ds_read_b128 v[178:181], v223 offset:49152
	ds_read_b128 v[182:185], v223 offset:57344
	s_waitcnt lgkmcnt(1)
	v_mfma_f32_32x32x16_bf16 v[112:127], v[178:181], v[130:133], v[112:127]
	v_pk_add_f32 v[88:89], v[64:65], v[66:67]
	v_pk_add_f32 v[90:91], v[72:73], v[74:75]
	v_pk_add_f32 v[234:235], v[80:81], v[82:83]
	v_pk_add_f32 v[236:237], v[194:195], v[196:197]
	v_pk_add_f32 v[88:89], v[68:69], v[88:89]
	v_pk_add_f32 v[90:91], v[76:77], v[90:91]
	v_pk_add_f32 v[234:235], v[84:85], v[234:235]
	v_pk_add_f32 v[236:237], v[92:93], v[236:237]
	v_pk_add_f32 v[88:89], v[70:71], v[88:89]
	v_pk_add_f32 v[90:91], v[78:79], v[90:91]
	v_pk_add_f32 v[234:235], v[86:87], v[234:235]
	v_pk_add_f32 v[236:237], v[94:95], v[236:237]
	v_pk_add_f32 v[88:89], v[88:89], v[90:91]
	v_pk_add_f32 v[234:235], v[234:235], v[236:237]
	v_pk_add_f32 v[88:89], v[88:89], v[234:235]
	v_add_f32_e32 v227, v88, v89
	v_mov_b32_e32 v228, v227
	v_cvt_pk_bf16_f32 v88, v64, v65
	v_cvt_pk_bf16_f32 v89, v66, v67
	v_cvt_pk_bf16_f32 v90, v68, v69
	v_cvt_pk_bf16_f32 v91, v70, v71
	s_nop 1
	v_permlane32_swap_b32_e32 v227, v228
	v_permlane32_swap_b32_e32 v88, v90
	v_permlane32_swap_b32_e32 v89, v91
	v_cvt_pk_bf16_f32 v72, v72, v73
	v_cvt_pk_bf16_f32 v73, v74, v75
	v_cvt_pk_bf16_f32 v74, v76, v77
	v_cvt_pk_bf16_f32 v75, v78, v79
	v_cvt_pk_bf16_f32 v64, v80, v81
	v_cvt_pk_bf16_f32 v65, v82, v83
	v_cvt_pk_bf16_f32 v66, v84, v85
	v_cvt_pk_bf16_f32 v67, v86, v87
	v_cvt_pk_bf16_f32 v68, v194, v195
	v_cvt_pk_bf16_f32 v69, v196, v197
	v_cvt_pk_bf16_f32 v70, v92, v93
	v_cvt_pk_bf16_f32 v71, v94, v95
	s_waitcnt lgkmcnt(0)
	v_mfma_f32_32x32x16_bf16 v[96:111], v[182:185], v[130:133], v[96:111]
	v_permlane32_swap_b32_e32 v72, v74
	v_permlane32_swap_b32_e32 v73, v75
	v_permlane32_swap_b32_e32 v64, v66
	v_permlane32_swap_b32_e32 v65, v67
	v_permlane32_swap_b32_e32 v68, v70
	v_permlane32_swap_b32_e32 v69, v71
	s_add_i32 s2, s39, -1
	s_mul_i32 s2, s2, s62
	s_lshl_b32 s72, s2, 6
	s_lshl_b64 s[2:3], s[72:73], 1
	s_add_u32 s12, s10, s2
	s_addc_u32 s13, s11, s3
	s_add_u32 s2, s8, s2
	s_addc_u32 s3, s9, s3
	global_load_dwordx4 v[178:181], v128, s[12:13]
	global_load_dwordx4 v[182:185], v198, s[12:13]
	global_load_dwordx4 v[186:189], v128, s[2:3]
	global_load_dwordx4 v[190:193], v198, s[2:3]
	ds_read_b64_tr_b16 v[76:77], v209 offset:0
	ds_read_b64_tr_b16 v[78:79], v209 offset:0x800
	ds_read_b64_tr_b16 v[80:81], v209 offset:0x1000
	ds_read_b64_tr_b16 v[82:83], v209 offset:0x1800
	ds_read_b64_tr_b16 v[84:85], v209 offset:0x2000
	ds_read_b64_tr_b16 v[86:87], v209 offset:0x2800
	ds_read_b64_tr_b16 v[92:93], v209 offset:0x3000
	ds_read_b64_tr_b16 v[94:95], v209 offset:0x3800
	s_waitcnt lgkmcnt(0)
	s_nop 0
	v_mfma_f32_32x32x16_bf16 v[0:15], v[76:79], v[88:91], v[0:15]
	v_mfma_f32_32x32x16_bf16 v[0:15], v[80:83], v[72:75], v[0:15]
	v_mfma_f32_32x32x16_bf16 v[0:15], v[84:87], v[64:67], v[0:15]
	ds_read_b64_tr_b16 v[76:77], v209 offset:0x200
	ds_read_b64_tr_b16 v[78:79], v209 offset:0xa00
	ds_read_b64_tr_b16 v[80:81], v209 offset:0x1200
	v_mfma_f32_32x32x16_bf16 v[0:15], v[92:95], v[68:71], v[0:15]
	ds_read_b64_tr_b16 v[82:83], v209 offset:0x1a00
	ds_read_b64_tr_b16 v[84:85], v209 offset:0x2200
	ds_read_b64_tr_b16 v[86:87], v209 offset:0x2a00
	ds_read_b64_tr_b16 v[92:93], v209 offset:0x3200
	ds_read_b64_tr_b16 v[94:95], v209 offset:0x3a00
	s_waitcnt lgkmcnt(0)
	v_mfma_f32_32x32x16_bf16 v[48:63], v[76:79], v[88:91], v[48:63]
	v_mfma_f32_32x32x16_bf16 v[48:63], v[80:83], v[72:75], v[48:63]
	v_mfma_f32_32x32x16_bf16 v[48:63], v[84:87], v[64:67], v[48:63]
	ds_read_b64_tr_b16 v[76:77], v209 offset:0x400
	ds_read_b64_tr_b16 v[78:79], v209 offset:0xc00
	ds_read_b64_tr_b16 v[80:81], v209 offset:0x1400
	ds_read_b64_tr_b16 v[82:83], v209 offset:0x1c00
	v_mfma_f32_32x32x16_bf16 v[48:63], v[92:95], v[68:71], v[48:63]
	ds_read_b64_tr_b16 v[84:85], v209 offset:0x2400
	ds_read_b64_tr_b16 v[86:87], v209 offset:0x2c00
	ds_read_b64_tr_b16 v[92:93], v209 offset:0x3400
	ds_read_b64_tr_b16 v[94:95], v209 offset:0x3c00
	s_waitcnt lgkmcnt(0)
	v_mfma_f32_32x32x16_bf16 v[32:47], v[76:79], v[88:91], v[32:47]
	ds_read_b64_tr_b16 v[76:77], v209 offset:0x600
	ds_read_b64_tr_b16 v[78:79], v209 offset:0xe00
	v_exp_f32_e32 v234, v104
	v_exp_f32_e32 v235, v105
	v_exp_f32_e32 v236, v106
	v_exp_f32_e32 v237, v107
	v_exp_f32_e32 v238, v108
	v_exp_f32_e32 v239, v109
	v_exp_f32_e32 v240, v110
	v_exp_f32_e32 v241, v111
	v_mfma_f32_32x32x16_bf16 v[32:47], v[80:83], v[72:75], v[32:47]
	v_exp_f32_e32 v80, v112
	v_exp_f32_e32 v81, v113
	v_exp_f32_e32 v82, v114
	v_exp_f32_e32 v83, v115
	v_mfma_f32_32x32x16_bf16 v[32:47], v[84:87], v[64:67], v[32:47]
	v_exp_f32_e32 v84, v116
	v_exp_f32_e32 v85, v117
	v_exp_f32_e32 v86, v118
	v_exp_f32_e32 v87, v119
	v_exp_f32_e32 v112, v96
	v_exp_f32_e32 v113, v97
	v_exp_f32_e32 v114, v98
	v_exp_f32_e32 v115, v99
	v_exp_f32_e32 v116, v100
	v_exp_f32_e32 v117, v101
	v_exp_f32_e32 v118, v102
	v_exp_f32_e32 v119, v103
	v_mfma_f32_32x32x16_bf16 v[32:47], v[92:95], v[68:71], v[32:47]
	ds_read_b64_tr_b16 v[92:93], v209 offset:0x1600
	ds_read_b64_tr_b16 v[94:95], v209 offset:0x1e00
	ds_read_b64_tr_b16 v[96:97], v209 offset:0x2600
	ds_read_b64_tr_b16 v[98:99], v209 offset:0x2e00
	ds_read_b64_tr_b16 v[100:101], v209 offset:0x3600
	ds_read_b64_tr_b16 v[102:103], v209 offset:0x3e00
	s_waitcnt lgkmcnt(0)
	v_mfma_f32_32x32x16_bf16 v[16:31], v[76:79], v[88:91], v[16:31]
	v_exp_f32_e32 v88, v120
	v_exp_f32_e32 v89, v121
	v_exp_f32_e32 v90, v122
	v_exp_f32_e32 v91, v123
	v_mfma_f32_32x32x16_bf16 v[16:31], v[92:95], v[72:75], v[16:31]
	v_exp_f32_e32 v92, v124
	v_exp_f32_e32 v93, v125
	v_exp_f32_e32 v94, v126
	v_exp_f32_e32 v95, v127
	s_barrier
	v_mfma_f32_32x32x16_bf16 v[16:31], v[96:99], v[64:67], v[16:31]
	s_waitcnt vmcnt(4)
	ds_write_b128 v212, v[162:165]
	ds_write_b128 v213, v[166:169]
	ds_write_b128 v214, v[170:173] offset:32768
	ds_write_b128 v215, v[174:177] offset:32768
	v_mfma_f32_32x32x16_bf16 v[16:31], v[100:103], v[68:71], v[16:31]
.LBB0_883:
	s_waitcnt lgkmcnt(0)
	s_barrier
	ds_read_b128 v[64:67], v216 offset:32768
	ds_read_b128 v[68:71], v216 offset:40960
	ds_read_b128 v[162:165], v218 offset:32768
	ds_read_b128 v[166:169], v218 offset:40960
	s_waitcnt lgkmcnt(3)
	v_mfma_f32_32x32x16_bf16 v[96:111], v[64:67], v[138:141], 0
	s_waitcnt lgkmcnt(2)
	v_mfma_f32_32x32x16_bf16 v[64:79], v[68:71], v[138:141], 0
	s_waitcnt lgkmcnt(1)
	v_mfma_f32_32x32x16_bf16 v[96:111], v[162:165], v[154:157], v[96:111]
	s_waitcnt lgkmcnt(0)
	v_mfma_f32_32x32x16_bf16 v[64:79], v[166:169], v[154:157], v[64:79]
	ds_read_b128 v[162:165], v219 offset:32768
	ds_read_b128 v[166:169], v219 offset:40960
	s_waitcnt lgkmcnt(1)
	v_mfma_f32_32x32x16_bf16 v[96:111], v[162:165], v[158:161], v[96:111]
	s_waitcnt lgkmcnt(0)
	v_mfma_f32_32x32x16_bf16 v[64:79], v[166:169], v[158:161], v[64:79]
	ds_read_b128 v[162:165], v220 offset:32768
	ds_read_b128 v[166:169], v220 offset:40960
	s_waitcnt lgkmcnt(1)
	v_mfma_f32_32x32x16_bf16 v[96:111], v[162:165], v[150:153], v[96:111]
	s_waitcnt lgkmcnt(0)
	v_mfma_f32_32x32x16_bf16 v[64:79], v[166:169], v[150:153], v[64:79]
	ds_read_b128 v[162:165], v221 offset:32768
	ds_read_b128 v[166:169], v221 offset:40960
	s_waitcnt lgkmcnt(1)
	v_mfma_f32_32x32x16_bf16 v[96:111], v[162:165], v[146:149], v[96:111]
	s_waitcnt lgkmcnt(0)
	v_mfma_f32_32x32x16_bf16 v[64:79], v[166:169], v[146:149], v[64:79]
	ds_read_b128 v[162:165], v222 offset:32768
	ds_read_b128 v[166:169], v222 offset:40960
	s_waitcnt lgkmcnt(1)
	v_mfma_f32_32x32x16_bf16 v[96:111], v[162:165], v[142:145], v[96:111]
	s_waitcnt lgkmcnt(0)
	v_mfma_f32_32x32x16_bf16 v[64:79], v[166:169], v[142:145], v[64:79]
	ds_read_b128 v[162:165], v224 offset:32768
	ds_read_b128 v[166:169], v224 offset:40960
	s_waitcnt lgkmcnt(1)
	v_mfma_f32_32x32x16_bf16 v[96:111], v[162:165], v[134:137], v[96:111]
	s_waitcnt lgkmcnt(0)
	v_mfma_f32_32x32x16_bf16 v[64:79], v[166:169], v[134:137], v[64:79]
	ds_read_b128 v[162:165], v223 offset:32768
	ds_read_b128 v[166:169], v223 offset:40960
	s_waitcnt lgkmcnt(1)
	v_mfma_f32_32x32x16_bf16 v[96:111], v[162:165], v[130:133], v[96:111]
	s_waitcnt lgkmcnt(0)
	v_mfma_f32_32x32x16_bf16 v[64:79], v[166:169], v[130:133], v[64:79]
	v_pk_add_f32 v[120:121], v[80:81], v[82:83]
	v_pk_add_f32 v[122:123], v[88:89], v[90:91]
	v_pk_add_f32 v[194:195], v[112:113], v[114:115]
	v_pk_add_f32 v[196:197], v[234:235], v[236:237]
	v_pk_add_f32 v[120:121], v[84:85], v[120:121]
	v_pk_add_f32 v[122:123], v[92:93], v[122:123]
	v_pk_add_f32 v[194:195], v[116:117], v[194:195]
	v_pk_add_f32 v[196:197], v[238:239], v[196:197]
	v_pk_add_f32 v[120:121], v[86:87], v[120:121]
	v_pk_add_f32 v[122:123], v[94:95], v[122:123]
	v_pk_add_f32 v[194:195], v[118:119], v[194:195]
	v_pk_add_f32 v[196:197], v[240:241], v[196:197]
	v_pk_add_f32 v[120:121], v[120:121], v[122:123]
	v_pk_add_f32 v[194:195], v[194:195], v[196:197]
	v_pk_add_f32 v[120:121], v[120:121], v[194:195]
	v_add_f32_e32 v229, v120, v121
	v_mov_b32_e32 v233, v229
	s_nop 1
	v_permlane32_swap_b32_e32 v229, v233
	v_cvt_pk_bf16_f32 v124, v80, v81
	v_cvt_pk_bf16_f32 v125, v82, v83
	v_cvt_pk_bf16_f32 v126, v84, v85
	v_cvt_pk_bf16_f32 v127, v86, v87
	v_cvt_pk_bf16_f32 v120, v88, v89
	v_cvt_pk_bf16_f32 v121, v90, v91
	v_cvt_pk_bf16_f32 v122, v92, v93
	v_cvt_pk_bf16_f32 v123, v94, v95
	v_cvt_pk_bf16_f32 v112, v112, v113
	v_cvt_pk_bf16_f32 v113, v114, v115
	v_cvt_pk_bf16_f32 v114, v116, v117
	v_cvt_pk_bf16_f32 v115, v118, v119
	v_cvt_pk_bf16_f32 v116, v234, v235
	v_cvt_pk_bf16_f32 v117, v236, v237
	v_cvt_pk_bf16_f32 v118, v238, v239
	v_cvt_pk_bf16_f32 v119, v240, v241
	s_nop 0
	v_permlane32_swap_b32_e32 v124, v126
	v_permlane32_swap_b32_e32 v125, v127
	v_permlane32_swap_b32_e32 v120, v122
	v_permlane32_swap_b32_e32 v121, v123
	v_permlane32_swap_b32_e32 v112, v114
	v_permlane32_swap_b32_e32 v113, v115
	v_permlane32_swap_b32_e32 v116, v118
	v_permlane32_swap_b32_e32 v117, v119
	s_min_i32 s2, s39, s14
	s_mul_i32 s2, s2, s62
	s_lshl_b32 s72, s2, 6
	s_lshl_b64 s[2:3], s[72:73], 1
	s_add_u32 s12, s10, s2
	s_addc_u32 s13, s11, s3
	s_add_u32 s2, s8, s2
	s_addc_u32 s3, s9, s3
	global_load_dwordx4 v[162:165], v128, s[12:13]
	global_load_dwordx4 v[166:169], v198, s[12:13]
	global_load_dwordx4 v[170:173], v128, s[2:3]
	global_load_dwordx4 v[174:177], v198, s[2:3]
	ds_read_b64_tr_b16 v[80:81], v211 offset:0
	ds_read_b64_tr_b16 v[82:83], v211 offset:0x800
	ds_read_b64_tr_b16 v[84:85], v211 offset:0x1000
	ds_read_b64_tr_b16 v[86:87], v211 offset:0x1800
	ds_read_b64_tr_b16 v[88:89], v211 offset:0x2000
	ds_read_b64_tr_b16 v[90:91], v211 offset:0x2800
	ds_read_b64_tr_b16 v[92:93], v211 offset:0x3000
	ds_read_b64_tr_b16 v[94:95], v211 offset:0x3800
	s_waitcnt lgkmcnt(0)
	s_nop 0
	v_mfma_f32_32x32x16_bf16 v[0:15], v[80:83], v[124:127], v[0:15]
	v_mfma_f32_32x32x16_bf16 v[0:15], v[84:87], v[120:123], v[0:15]
	v_mfma_f32_32x32x16_bf16 v[0:15], v[88:91], v[112:115], v[0:15]
	ds_read_b64_tr_b16 v[80:81], v211 offset:0x200
	ds_read_b64_tr_b16 v[82:83], v211 offset:0xa00
	ds_read_b64_tr_b16 v[84:85], v211 offset:0x1200
	v_mfma_f32_32x32x16_bf16 v[0:15], v[92:95], v[116:119], v[0:15]
	ds_read_b64_tr_b16 v[86:87], v211 offset:0x1a00
	ds_read_b64_tr_b16 v[88:89], v211 offset:0x2200
	ds_read_b64_tr_b16 v[90:91], v211 offset:0x2a00
	ds_read_b64_tr_b16 v[92:93], v211 offset:0x3200
	ds_read_b64_tr_b16 v[94:95], v211 offset:0x3a00
	s_waitcnt lgkmcnt(0)
	v_mfma_f32_32x32x16_bf16 v[48:63], v[80:83], v[124:127], v[48:63]
	v_mfma_f32_32x32x16_bf16 v[48:63], v[84:87], v[120:123], v[48:63]
	v_mfma_f32_32x32x16_bf16 v[48:63], v[88:91], v[112:115], v[48:63]
	ds_read_b64_tr_b16 v[80:81], v211 offset:0x400
	ds_read_b64_tr_b16 v[82:83], v211 offset:0xc00
	ds_read_b64_tr_b16 v[84:85], v211 offset:0x1400
	ds_read_b64_tr_b16 v[86:87], v211 offset:0x1c00
	v_mfma_f32_32x32x16_bf16 v[48:63], v[92:95], v[116:119], v[48:63]
	ds_read_b64_tr_b16 v[88:89], v211 offset:0x2400
	ds_read_b64_tr_b16 v[90:91], v211 offset:0x2c00
	ds_read_b64_tr_b16 v[92:93], v211 offset:0x3400
	ds_read_b64_tr_b16 v[94:95], v211 offset:0x3c00
	s_waitcnt lgkmcnt(0)
	v_mfma_f32_32x32x16_bf16 v[32:47], v[80:83], v[124:127], v[32:47]
	v_exp_f32_e32 v80, v64
	v_exp_f32_e32 v81, v65
	v_exp_f32_e32 v64, v96
	v_exp_f32_e32 v65, v97
	v_exp_f32_e32 v82, v66
	v_exp_f32_e32 v83, v67
	v_exp_f32_e32 v66, v98
	v_exp_f32_e32 v67, v99
	v_mfma_f32_32x32x16_bf16 v[32:47], v[84:87], v[120:123], v[32:47]
	v_exp_f32_e32 v84, v68
	v_exp_f32_e32 v85, v69
	v_exp_f32_e32 v68, v100
	v_exp_f32_e32 v69, v101
	v_exp_f32_e32 v86, v70
	v_exp_f32_e32 v87, v71
	v_exp_f32_e32 v70, v102
	v_exp_f32_e32 v71, v103
	v_mfma_f32_32x32x16_bf16 v[32:47], v[88:91], v[112:115], v[32:47]
	v_exp_f32_e32 v194, v72
	v_exp_f32_e32 v195, v73
	ds_read_b64_tr_b16 v[72:73], v211 offset:0x600
	v_exp_f32_e32 v196, v74
	v_exp_f32_e32 v197, v75
	ds_read_b64_tr_b16 v[74:75], v211 offset:0xe00
	v_mfma_f32_32x32x16_bf16 v[32:47], v[92:95], v[116:119], v[32:47]
	v_exp_f32_e32 v92, v76
	v_exp_f32_e32 v93, v77
	ds_read_b64_tr_b16 v[76:77], v211 offset:0x1600
	v_exp_f32_e32 v94, v78
	v_exp_f32_e32 v95, v79
	ds_read_b64_tr_b16 v[78:79], v211 offset:0x1e00
	ds_read_b64_tr_b16 v[96:97], v211 offset:0x2600
	ds_read_b64_tr_b16 v[98:99], v211 offset:0x2e00
	ds_read_b64_tr_b16 v[100:101], v211 offset:0x3600
	ds_read_b64_tr_b16 v[102:103], v211 offset:0x3e00
	s_waitcnt lgkmcnt(0)
	v_mfma_f32_32x32x16_bf16 v[16:31], v[72:75], v[124:127], v[16:31]
	v_exp_f32_e32 v72, v104
	v_exp_f32_e32 v73, v105
	v_exp_f32_e32 v74, v106
	v_exp_f32_e32 v75, v107
	v_mfma_f32_32x32x16_bf16 v[16:31], v[76:79], v[120:123], v[16:31]
	v_exp_f32_e32 v76, v108
	v_exp_f32_e32 v77, v109
	v_exp_f32_e32 v78, v110
	v_exp_f32_e32 v79, v111
	s_barrier
	v_mfma_f32_32x32x16_bf16 v[16:31], v[96:99], v[112:115], v[16:31]
	s_waitcnt vmcnt(4)
	ds_write_b128 v212, v[178:181] offset:16384
	ds_write_b128 v213, v[182:185] offset:16384
	ds_write_b128 v214, v[186:189] offset:49152
	ds_write_b128 v215, v[190:193] offset:49152
	v_mfma_f32_32x32x16_bf16 v[16:31], v[100:103], v[116:119], v[16:31]
